# P19 bf16 GEMM also uses the 8-row x 128-B LDS subtile image (full-line LDS-DMA fetches)
# baseline (speedup 1.0000x reference)
.LBB0_1359:
	s_waitcnt vmcnt(0)
	v_lshrrev_b32_e32 v4, 1, v0
	s_add_u32 s33, s82, 0x4b00000
	v_and_b32_e32 v13, 24, v4
	v_lshrrev_b32_e32 v4, 5, v0
	s_addc_u32 s34, s83, 0
	v_lshlrev_b32_e32 v2, 4, v0
	v_and_b32_e32 v3, 32, v0
	v_and_b32_e32 v4, 4, v4
	v_bfe_u32 v5, v0, 2, 2
	s_add_i32 s0, s6, s0
	v_bfe_u32 v12, v0, 2, 4
	v_bitop3_b32 v10, v2, v3, 48 bitop3:0x6c
	v_and_b32_e32 v11, 64, v0
	v_or3_b32 v4, v4, v5, v13
	v_lshrrev_b32_e32 v5, 3, v0
	v_or_b32_e32 v14, 0x2000, v2
	s_ashr_i32 s6, s0, 31
	v_or_b32_e32 v3, v10, v11
	v_and_or_b32 v6, v5, 48, v12
	v_and_or_b32 v5, v5, 32, v4
	v_lshrrev_b32_e32 v2, 7, v14
	s_movk_i32 s7, 0x70
	s_lshr_b32 s6, s6, 26
	v_lshl_or_b32 v132, v5, 12, v3
	v_and_or_b32 v5, v2, s7, v12
	s_movk_i32 s7, 0x60
	s_add_i32 s6, s0, s6
	v_and_or_b32 v2, v2, s7, v4
	s_ashr_i32 s7, s6, 6
	s_and_b32 s6, s6, 0xffc0
	s_sub_i32 s6, s0, s6
	s_bfe_i32 s0, s6, 0x80000
	s_bfe_u32 s0, s0, 0x3000c
	s_add_i32 s9, s6, s0
	s_bfe_i32 s0, s9, 0x80000
	s_and_b32 s9, s9, 0xf8
	s_sub_i32 s6, s6, s9
	s_lshl_b32 s7, s7, 3
	s_sext_i32_i16 s0, s0
	s_sext_i32_i8 s6, s6
	s_lshr_b32 s1, s2, 8
	s_lshr_b32 s0, s0, 3
	s_add_i32 s16, s7, s6
	s_lshr_b32 s8, s2, 6
	s_ashr_i32 s17, s16, 31
	s_bfe_i64 s[10:11], s[0:1], 0x100000
	s_lshl_b32 s35, s8, 10
	s_lshl_b64 s[6:7], s[16:17], 20
	s_lshl_b64 s[10:11], s[10:11], 20
	s_add_u32 s28, s33, s10
	s_addc_u32 s29, s34, s11
	s_add_i32 s17, s35, 0
	s_add_i32 m0, s17, 0x10000
	v_readlane_b32 s9, v254, 36
	v_lshrrev_b32_e32 v236, 3, v204
	v_and_b32_e32 v237, 7, v204
	v_xor_b32_e32 v237, v237, v236
	v_lshlrev_b32_e32 v237, 4, v237
	v_mov_b32_e32 v239, s89
	v_lshl_add_u32 v238, v239, 3, v236
	v_lshl_or_b32 v130, v238, 12, v237
	v_add_u32_e32 v134, 0x40000, v130
	v_and_b32_e32 v240, 1, v239
	v_lshlrev_b32_e32 v240, 4, v240
	v_bfe_u32 v241, v239, 1, 1
	v_lshlrev_b32_e32 v241, 2, v241
	v_lshrrev_b32_e32 v242, 2, v239
	v_lshlrev_b32_e32 v242, 5, v242
	v_bfe_u32 v243, v236, 2, 1
	v_lshlrev_b32_e32 v243, 3, v243
	v_and_b32_e32 v244, 3, v236
	v_add3_u32 v240, v240, v241, v242
	v_add3_u32 v240, v240, v243, v244
	v_lshl_or_b32 v132, v240, 12, v237
	v_add_u32_e32 v136, 0x40000, v132
	global_load_lds_dwordx4 v132, s[28:29]
	s_add_i32 m0, s17, 0x12000
	s_nop 0
	s_add_u32 s26, s9, s6
	v_readlane_b32 s6, v254, 37
	s_nop 0
	global_load_lds_dwordx4 v136, s[28:29]
	s_addc_u32 s27, s6, s7
	s_mov_b32 m0, s17
	s_add_i32 s36, s17, 0x2000
	s_nop 0
	global_load_lds_dwordx4 v130, s[26:27]
	s_mov_b32 m0, s36
	s_add_u32 s6, s28, 0x80000
	global_load_lds_dwordx4 v134, s[26:27]
	s_addc_u32 s7, s29, 0
	s_add_i32 m0, s17, 0x14000
	v_mov_b32_e32 v133, 0
	global_load_lds_dwordx4 v132, s[6:7]
	s_add_i32 m0, s17, 0x16000
	v_mov_b32_e32 v137, v133
	global_load_lds_dwordx4 v136, s[6:7]
	s_add_u32 s6, s26, 0x80000
	s_addc_u32 s7, s27, 0
	s_add_i32 s37, s17, 0x4000
	s_mov_b32 m0, s37
	s_add_i32 s38, s17, 0x6000
	global_load_lds_dwordx4 v130, s[6:7]
	s_mov_b32 m0, s38
	v_mov_b32_e32 v131, v133
	global_load_lds_dwordx4 v134, s[6:7]
	v_mov_b32_e32 v135, v133
	s_mov_b32 s39, 0
	v_lshl_add_u64 v[8:9], s[28:29], 0, v[132:133]
	v_lshl_add_u64 v[6:7], s[28:29], 0, v[136:137]
	v_lshl_add_u64 v[4:5], s[26:27], 0, v[130:131]
	v_lshl_add_u64 v[2:3], s[26:27], 0, v[134:135]
	s_cmp_lg_u32 s1, 1
	s_mov_b64 s[6:7], 0x80000
	s_cbranch_scc1 .LBB0_1361
	s_barrier
.LBB0_1361:
	s_lshl_b32 s8, s8, 5
	s_and_b32 s13, s8, 0x60
	s_mov_b64 s[8:9], 0x80
	s_add_i32 m0, s17, 0x18000
	v_lshl_add_u64 v[8:9], v[8:9], 0, s[8:9]
	s_lshl_b32 s12, s1, 13
	s_lshl_b32 s14, s13, 7
	s_waitcnt vmcnt(4)
	s_barrier
	global_load_lds_dwordx4 v[8:9], off
	v_lshl_add_u64 v[6:7], v[6:7], 0, s[8:9]
	s_add_i32 m0, s17, 0x1a000
	s_add_i32 s40, s17, 0x8000
	s_add_i32 s41, s17, 0xa000
	global_load_lds_dwordx4 v[6:7], off
	v_lshl_add_u64 v[4:5], v[4:5], 0, s[8:9]
	s_mov_b32 m0, s40
	s_add_u32 s10, s28, 0x80080
	global_load_lds_dwordx4 v[4:5], off
	v_lshl_add_u64 v[2:3], v[2:3], 0, s[8:9]
	s_mov_b32 m0, s41
	s_addc_u32 s11, s29, 0
	global_load_lds_dwordx4 v[2:3], off
	s_add_i32 m0, s17, 0x1c000
	v_lshl_add_u64 v[2:3], s[10:11], 0, v[132:133]
	global_load_lds_dwordx4 v[2:3], off
	v_lshl_add_u64 v[2:3], s[10:11], 0, v[136:137]
	s_add_i32 m0, s17, 0x1e000
	s_sext_i32_i8 s49, s0
	global_load_lds_dwordx4 v[2:3], off
	v_lshlrev_b32_e32 v2, 1, v13
	v_lshlrev_b32_e32 v4, 2, v0
	v_lshlrev_b32_e32 v5, 6, v0
	s_movk_i32 s0, 0x3c0
	v_lshl_or_b32 v3, v209, 6, v2
	v_and_b32_e32 v4, 32, v4
	v_and_or_b32 v2, v5, s0, v2
	v_bitop3_b32 v147, s14, v2, v4 bitop3:0xf6
	v_lshlrev_b32_e32 v2, 9, v0
	v_bitop3_b32 v3, v3, s12, v4 bitop3:0xde
	v_and_b32_e32 v2, 0x30000, v2
	v_lshlrev_b32_e32 v4, 12, v12
	v_or3_b32 v2, v10, v2, v4
	v_mov_b32_e32 v138, v130
	v_lshlrev_b32_e32 v2, 5, v14
	s_waitcnt vmcnt(6)
	v_and_b32_e32 v2, 0x70000, v2
	v_lshl_or_b32 v146, s1, 6, v209
	v_readlane_b32 s0, v254, 42
	v_or3_b32 v2, v10, v2, v4
	s_add_i32 s43, 0, 0x10000
	s_add_i32 s44, 0, 0x14000
	s_ashr_i32 s42, s0, 31
	v_or_b32_e32 v148, s13, v13
	v_mov_b32_e32 v139, v133
	v_mov_b32_e32 v140, v134
	v_mov_b32_e32 v141, v133
	v_mov_b64_e32 v[142:143], 0x400
	v_mov_b64_e32 v[144:145], 0x3ff
	v_add_u32_e32 v149, s43, v147
	v_add_u32_e32 v150, 0, v3
	v_add_u32_e32 v151, s44, v147
	v_and_b32_e32 v236, 15, v204
	v_lshrrev_b32_e32 v237, 4, v204
	v_and_b32_e32 v238, 7, v236
	v_xor_b32_e32 v237, v237, v238
	v_lshlrev_b32_e32 v237, 4, v237
	v_lshl_or_b32 v237, v238, 7, v237
	v_lshrrev_b32_e32 v238, 3, v236
	v_lshl_or_b32 v237, v238, 10, v237
	v_add_u32_e32 v150, s12, v237
	v_add_u32_e32 v147, s14, v237
	v_add_u32_e32 v149, s43, v147
	v_add_u32_e32 v151, s44, v147
	v_xor_b32_e32 v245, 64, v150
	v_xor_b32_e32 v246, 64, v149
	v_xor_b32_e32 v247, 64, v151
	s_mov_b32 s45, 0x80000
	s_mov_b64 s[10:11], 0x90000
	s_mov_b32 s46, 0x90000
	s_mov_b64 s[12:13], 0xa0000
	s_mov_b32 s47, 0xa0000
	s_mov_b64 s[14:15], 0xb0000
	s_mov_b32 s48, 0xb0000
	s_barrier
	v_readlane_b32 s1, v254, 43

.LBB0_1369:
	ds_read_b128 v[152:155], v149
	ds_read_b128 v[156:159], v246
	ds_read_b128 v[160:163], v149 offset:2048
	ds_read_b128 v[164:167], v246 offset:2048
	s_add_u32 s28, s26, 0xfff80080
	s_addc_u32 s29, s27, -1
	s_cmp_eq_u32 s54, 28
	s_cselect_b32 s31, s21, s29
	s_cselect_b32 s30, s50, s28
	s_cselect_b32 s29, s19, s53
	s_cselect_b32 s28, s51, s52
	v_lshl_add_u64 v[202:203], s[26:27], 0, v[138:139]
	s_add_i32 m0, s17, 0xc000
	ds_read_b128 v[168:171], v150
	ds_read_b128 v[172:175], v245
	ds_read_b128 v[176:179], v150 offset:2048
	ds_read_b128 v[180:183], v245 offset:2048
	ds_read_b128 v[184:187], v150 offset:4096
	ds_read_b128 v[190:193], v245 offset:4096
	ds_read_b128 v[194:197], v150 offset:6144
	ds_read_b128 v[198:201], v245 offset:6144
	global_load_lds_dwordx4 v[202:203], off
	v_lshl_add_u64 v[202:203], s[26:27], 0, v[140:141]
	s_add_i32 m0, s17, 0xe000
	s_nop 0
	global_load_lds_dwordx4 v[202:203], off
	s_waitcnt lgkmcnt(8)
	s_barrier
	s_waitcnt lgkmcnt(0)
	s_setprio 1
	s_waitcnt lgkmcnt(0)
	v_mfma_f32_16x16x32_bf16 v[126:129], v[152:155], v[168:171], v[126:129]
	v_mfma_f32_16x16x32_bf16 v[122:125], v[160:163], v[168:171], v[122:125]
	v_mfma_f32_16x16x32_bf16 v[118:121], v[152:155], v[176:179], v[118:121]
	v_mfma_f32_16x16x32_bf16 v[114:117], v[160:163], v[176:179], v[114:117]
	v_mfma_f32_16x16x32_bf16 v[102:105], v[152:155], v[184:187], v[102:105]
	v_mfma_f32_16x16x32_bf16 v[98:101], v[160:163], v[184:187], v[98:101]
	v_mfma_f32_16x16x32_bf16 v[86:89], v[152:155], v[194:197], v[86:89]
	v_mfma_f32_16x16x32_bf16 v[82:85], v[160:163], v[194:197], v[82:85]
	v_mfma_f32_16x16x32_bf16 v[126:129], v[156:159], v[172:175], v[126:129]
	v_mfma_f32_16x16x32_bf16 v[122:125], v[164:167], v[172:175], v[122:125]
	v_mfma_f32_16x16x32_bf16 v[118:121], v[156:159], v[180:183], v[118:121]
	v_mfma_f32_16x16x32_bf16 v[114:117], v[164:167], v[180:183], v[114:117]
	v_mfma_f32_16x16x32_bf16 v[102:105], v[156:159], v[190:193], v[102:105]
	v_mfma_f32_16x16x32_bf16 v[98:101], v[164:167], v[190:193], v[98:101]
	v_mfma_f32_16x16x32_bf16 v[86:89], v[156:159], v[198:201], v[86:89]
	v_mfma_f32_16x16x32_bf16 v[82:85], v[164:167], v[198:201], v[82:85]
	s_setprio 0
	s_barrier
	s_add_i32 s55, s43, s35
	v_lshl_add_u64 v[202:203], s[28:29], 0, v[132:133]
	s_mov_b32 m0, s55
	ds_read_b128 v[214:217], v151
	ds_read_b128 v[218:221], v247
	ds_read_b128 v[222:225], v151 offset:2048
	ds_read_b128 v[226:229], v247 offset:2048
	global_load_lds_dwordx4 v[202:203], off
	v_lshl_add_u64 v[230:231], s[28:29], 0, v[136:137]
	s_add_i32 m0, s55, 0x2000
	s_nop 0
	global_load_lds_dwordx4 v[230:231], off
	s_barrier
	s_waitcnt lgkmcnt(0)
	s_setprio 1
	s_waitcnt lgkmcnt(0)
	v_mfma_f32_16x16x32_bf16 v[110:113], v[214:217], v[168:171], v[110:113]
	v_mfma_f32_16x16x32_bf16 v[106:109], v[222:225], v[168:171], v[106:109]
	v_mfma_f32_16x16x32_bf16 v[94:97], v[214:217], v[176:179], v[94:97]
	v_mfma_f32_16x16x32_bf16 v[90:93], v[222:225], v[176:179], v[90:93]
	v_mfma_f32_16x16x32_bf16 v[78:81], v[214:217], v[184:187], v[78:81]
	v_mfma_f32_16x16x32_bf16 v[74:77], v[222:225], v[184:187], v[74:77]
	v_mfma_f32_16x16x32_bf16 v[70:73], v[214:217], v[194:197], v[70:73]
	v_mfma_f32_16x16x32_bf16 v[66:69], v[222:225], v[194:197], v[66:69]
	v_mfma_f32_16x16x32_bf16 v[110:113], v[218:221], v[172:175], v[110:113]
	v_mfma_f32_16x16x32_bf16 v[106:109], v[226:229], v[172:175], v[106:109]
	v_mfma_f32_16x16x32_bf16 v[94:97], v[218:221], v[180:183], v[94:97]
	v_mfma_f32_16x16x32_bf16 v[90:93], v[226:229], v[180:183], v[90:93]
	v_mfma_f32_16x16x32_bf16 v[78:81], v[218:221], v[190:193], v[78:81]
	v_mfma_f32_16x16x32_bf16 v[74:77], v[226:229], v[190:193], v[74:77]
	v_mfma_f32_16x16x32_bf16 v[70:73], v[218:221], v[198:201], v[70:73]
	v_mfma_f32_16x16x32_bf16 v[66:69], v[226:229], v[198:201], v[66:69]
	s_setprio 0
	s_mov_b32 m0, s17
	v_lshl_add_u64 v[232:233], s[30:31], 0, v[130:131]
	s_barrier
	ds_read_b128 v[168:171], v150 offset:16384
	ds_read_b128 v[172:175], v245 offset:16384
	ds_read_b128 v[176:179], v150 offset:18432
	ds_read_b128 v[180:183], v245 offset:18432
	ds_read_b128 v[184:187], v150 offset:20480
	ds_read_b128 v[190:193], v245 offset:20480
	ds_read_b128 v[194:197], v150 offset:22528
	ds_read_b128 v[198:201], v245 offset:22528
	global_load_lds_dwordx4 v[232:233], off
	v_lshl_add_u64 v[234:235], s[30:31], 0, v[134:135]
	s_mov_b32 m0, s36
	s_nop 0
	global_load_lds_dwordx4 v[234:235], off
	s_barrier
	s_waitcnt lgkmcnt(0)
	s_setprio 1
	s_waitcnt lgkmcnt(0)
	v_mfma_f32_16x16x32_bf16 v[62:65], v[152:155], v[168:171], v[62:65]
	v_mfma_f32_16x16x32_bf16 v[58:61], v[160:163], v[168:171], v[58:61]
	v_mfma_f32_16x16x32_bf16 v[54:57], v[152:155], v[176:179], v[54:57]
	v_mfma_f32_16x16x32_bf16 v[50:53], v[160:163], v[176:179], v[50:53]
	v_mfma_f32_16x16x32_bf16 v[38:41], v[152:155], v[184:187], v[38:41]
	v_mfma_f32_16x16x32_bf16 v[34:37], v[160:163], v[184:187], v[34:37]
	v_mfma_f32_16x16x32_bf16 v[22:25], v[152:155], v[194:197], v[22:25]
	v_mfma_f32_16x16x32_bf16 v[18:21], v[160:163], v[194:197], v[18:21]
	v_mfma_f32_16x16x32_bf16 v[62:65], v[156:159], v[172:175], v[62:65]
	v_mfma_f32_16x16x32_bf16 v[58:61], v[164:167], v[172:175], v[58:61]
	v_mfma_f32_16x16x32_bf16 v[54:57], v[156:159], v[180:183], v[54:57]
	v_mfma_f32_16x16x32_bf16 v[50:53], v[164:167], v[180:183], v[50:53]
	v_mfma_f32_16x16x32_bf16 v[38:41], v[156:159], v[190:193], v[38:41]
	v_mfma_f32_16x16x32_bf16 v[34:37], v[164:167], v[190:193], v[34:37]
	v_mfma_f32_16x16x32_bf16 v[22:25], v[156:159], v[198:201], v[22:25]
	v_mfma_f32_16x16x32_bf16 v[18:21], v[164:167], v[198:201], v[18:21]
	s_setprio 0
	s_barrier
	s_add_u32 s56, s28, 0x80000
	s_addc_u32 s57, s29, 0
	s_add_i32 s55, s44, s35
	v_lshl_add_u64 v[152:153], s[56:57], 0, v[132:133]
	s_mov_b32 m0, s55
	s_nop 0
	global_load_lds_dwordx4 v[152:153], off
	v_lshl_add_u64 v[152:153], s[56:57], 0, v[136:137]
	s_add_i32 m0, s55, 0x2000
	s_nop 0
	global_load_lds_dwordx4 v[152:153], off
	s_waitcnt vmcnt(6)
	s_barrier
	s_setprio 1
	v_mfma_f32_16x16x32_bf16 v[46:49], v[214:217], v[168:171], v[46:49]
	v_mfma_f32_16x16x32_bf16 v[42:45], v[222:225], v[168:171], v[42:45]
	v_mfma_f32_16x16x32_bf16 v[30:33], v[214:217], v[176:179], v[30:33]
	v_mfma_f32_16x16x32_bf16 v[26:29], v[222:225], v[176:179], v[26:29]
	v_mfma_f32_16x16x32_bf16 v[14:17], v[214:217], v[184:187], v[14:17]
	v_mfma_f32_16x16x32_bf16 v[10:13], v[222:225], v[184:187], v[10:13]
	v_mfma_f32_16x16x32_bf16 v[6:9], v[214:217], v[194:197], v[6:9]
	v_mfma_f32_16x16x32_bf16 v[2:5], v[222:225], v[194:197], v[2:5]
	v_mfma_f32_16x16x32_bf16 v[46:49], v[218:221], v[172:175], v[46:49]
	v_mfma_f32_16x16x32_bf16 v[42:45], v[226:229], v[172:175], v[42:45]
	v_mfma_f32_16x16x32_bf16 v[30:33], v[218:221], v[180:183], v[30:33]
	v_mfma_f32_16x16x32_bf16 v[26:29], v[226:229], v[180:183], v[26:29]
	v_mfma_f32_16x16x32_bf16 v[14:17], v[218:221], v[190:193], v[14:17]
	v_mfma_f32_16x16x32_bf16 v[10:13], v[226:229], v[190:193], v[10:13]
	v_mfma_f32_16x16x32_bf16 v[6:9], v[218:221], v[198:201], v[6:9]
	v_mfma_f32_16x16x32_bf16 v[2:5], v[226:229], v[198:201], v[2:5]
	s_setprio 0
	s_add_i32 s55, 0, 0x18000
	v_add_u32_e32 v164, s55, v147
	v_xor_b32_e32 v248, 64, v164
	s_barrier
	ds_read_b128 v[152:155], v164
	ds_read_b128 v[156:159], v248
	ds_read_b128 v[160:163], v164 offset:2048
	ds_read_b128 v[164:167], v248 offset:2048
	s_add_u32 s30, s30, 0x80000
	s_addc_u32 s31, s31, 0
	s_mov_b32 m0, s37
	v_lshl_add_u64 v[214:215], s[30:31], 0, v[130:131]
	ds_read_b128 v[168:171], v150 offset:32768
	ds_read_b128 v[172:175], v245 offset:32768
	ds_read_b128 v[176:179], v150 offset:34816
	ds_read_b128 v[180:183], v245 offset:34816
	ds_read_b128 v[184:187], v150 offset:36864
	ds_read_b128 v[190:193], v245 offset:36864
	ds_read_b128 v[194:197], v150 offset:38912
	ds_read_b128 v[198:201], v245 offset:38912
	global_load_lds_dwordx4 v[214:215], off
	v_lshl_add_u64 v[214:215], s[30:31], 0, v[134:135]
	s_mov_b32 m0, s38
	s_nop 0
	global_load_lds_dwordx4 v[214:215], off
	s_waitcnt lgkmcnt(8)
	s_barrier
	s_waitcnt lgkmcnt(0)
	s_setprio 1
	s_waitcnt lgkmcnt(0)
	v_mfma_f32_16x16x32_bf16 v[126:129], v[152:155], v[168:171], v[126:129]
	v_mfma_f32_16x16x32_bf16 v[122:125], v[160:163], v[168:171], v[122:125]
	v_mfma_f32_16x16x32_bf16 v[118:121], v[152:155], v[176:179], v[118:121]
	v_mfma_f32_16x16x32_bf16 v[114:117], v[160:163], v[176:179], v[114:117]
	v_mfma_f32_16x16x32_bf16 v[102:105], v[152:155], v[184:187], v[102:105]
	v_mfma_f32_16x16x32_bf16 v[98:101], v[160:163], v[184:187], v[98:101]
	v_mfma_f32_16x16x32_bf16 v[86:89], v[152:155], v[194:197], v[86:89]
	v_mfma_f32_16x16x32_bf16 v[82:85], v[160:163], v[194:197], v[82:85]
	v_mfma_f32_16x16x32_bf16 v[126:129], v[156:159], v[172:175], v[126:129]
	v_mfma_f32_16x16x32_bf16 v[122:125], v[164:167], v[172:175], v[122:125]
	v_mfma_f32_16x16x32_bf16 v[118:121], v[156:159], v[180:183], v[118:121]
	v_mfma_f32_16x16x32_bf16 v[114:117], v[164:167], v[180:183], v[114:117]
	v_mfma_f32_16x16x32_bf16 v[102:105], v[156:159], v[190:193], v[102:105]
	v_mfma_f32_16x16x32_bf16 v[98:101], v[164:167], v[190:193], v[98:101]
	v_mfma_f32_16x16x32_bf16 v[86:89], v[156:159], v[198:201], v[86:89]
	v_mfma_f32_16x16x32_bf16 v[82:85], v[164:167], v[198:201], v[82:85]
	s_setprio 0
	s_barrier
	s_add_i32 s30, 0, 0x1c000
	s_add_i32 s31, s55, s35
	v_add_u32_e32 v213, s30, v147
	v_xor_b32_e32 v249, 64, v213
	v_lshl_add_u64 v[202:203], v[202:203], 0, s[8:9]
	s_mov_b32 m0, s31
	ds_read_b128 v[214:217], v213
	ds_read_b128 v[218:221], v249
	ds_read_b128 v[222:225], v213 offset:2048
	ds_read_b128 v[226:229], v249 offset:2048
	global_load_lds_dwordx4 v[202:203], off
	v_lshl_add_u64 v[202:203], v[230:231], 0, s[8:9]
	s_add_i32 m0, s31, 0x2000
	s_nop 0
	global_load_lds_dwordx4 v[202:203], off
	s_barrier
	s_waitcnt lgkmcnt(0)
	s_setprio 1
	s_waitcnt lgkmcnt(0)
	v_mfma_f32_16x16x32_bf16 v[110:113], v[214:217], v[168:171], v[110:113]
	v_mfma_f32_16x16x32_bf16 v[106:109], v[222:225], v[168:171], v[106:109]
	v_mfma_f32_16x16x32_bf16 v[94:97], v[214:217], v[176:179], v[94:97]
	v_mfma_f32_16x16x32_bf16 v[90:93], v[222:225], v[176:179], v[90:93]
	v_mfma_f32_16x16x32_bf16 v[78:81], v[214:217], v[184:187], v[78:81]
	v_mfma_f32_16x16x32_bf16 v[74:77], v[222:225], v[184:187], v[74:77]
	v_mfma_f32_16x16x32_bf16 v[70:73], v[214:217], v[194:197], v[70:73]
	v_mfma_f32_16x16x32_bf16 v[66:69], v[222:225], v[194:197], v[66:69]
	v_mfma_f32_16x16x32_bf16 v[110:113], v[218:221], v[172:175], v[110:113]
	v_mfma_f32_16x16x32_bf16 v[106:109], v[226:229], v[172:175], v[106:109]
	v_mfma_f32_16x16x32_bf16 v[94:97], v[218:221], v[180:183], v[94:97]
	v_mfma_f32_16x16x32_bf16 v[90:93], v[226:229], v[180:183], v[90:93]
	v_mfma_f32_16x16x32_bf16 v[78:81], v[218:221], v[190:193], v[78:81]
	v_mfma_f32_16x16x32_bf16 v[74:77], v[226:229], v[190:193], v[74:77]
	v_mfma_f32_16x16x32_bf16 v[70:73], v[218:221], v[198:201], v[70:73]
	v_mfma_f32_16x16x32_bf16 v[66:69], v[226:229], v[198:201], v[66:69]
	s_setprio 0
	s_mov_b32 m0, s40
	v_lshl_add_u64 v[202:203], v[232:233], 0, s[8:9]
	s_barrier
	ds_read_b128 v[168:171], v150 offset:49152
	ds_read_b128 v[172:175], v245 offset:49152
	ds_read_b128 v[176:179], v150 offset:51200
	ds_read_b128 v[180:183], v245 offset:51200
	ds_read_b128 v[184:187], v150 offset:53248
	ds_read_b128 v[190:193], v245 offset:53248
	ds_read_b128 v[194:197], v150 offset:55296
	ds_read_b128 v[198:201], v245 offset:55296
	global_load_lds_dwordx4 v[202:203], off
	v_lshl_add_u64 v[202:203], v[234:235], 0, s[8:9]
	s_mov_b32 m0, s41
	s_nop 0
	global_load_lds_dwordx4 v[202:203], off
	s_barrier
	s_waitcnt lgkmcnt(0)
	s_setprio 1
	s_waitcnt lgkmcnt(0)
	v_mfma_f32_16x16x32_bf16 v[62:65], v[152:155], v[168:171], v[62:65]
	v_mfma_f32_16x16x32_bf16 v[58:61], v[160:163], v[168:171], v[58:61]
	v_mfma_f32_16x16x32_bf16 v[54:57], v[152:155], v[176:179], v[54:57]
	v_mfma_f32_16x16x32_bf16 v[50:53], v[160:163], v[176:179], v[50:53]
	v_mfma_f32_16x16x32_bf16 v[38:41], v[152:155], v[184:187], v[38:41]
	v_mfma_f32_16x16x32_bf16 v[34:37], v[160:163], v[184:187], v[34:37]
	v_mfma_f32_16x16x32_bf16 v[22:25], v[152:155], v[194:197], v[22:25]
	v_mfma_f32_16x16x32_bf16 v[18:21], v[160:163], v[194:197], v[18:21]
	v_mfma_f32_16x16x32_bf16 v[62:65], v[156:159], v[172:175], v[62:65]
	v_mfma_f32_16x16x32_bf16 v[58:61], v[164:167], v[172:175], v[58:61]
	v_mfma_f32_16x16x32_bf16 v[54:57], v[156:159], v[180:183], v[54:57]
	v_mfma_f32_16x16x32_bf16 v[50:53], v[164:167], v[180:183], v[50:53]
	v_mfma_f32_16x16x32_bf16 v[38:41], v[156:159], v[190:193], v[38:41]
	v_mfma_f32_16x16x32_bf16 v[34:37], v[164:167], v[190:193], v[34:37]
	v_mfma_f32_16x16x32_bf16 v[22:25], v[156:159], v[198:201], v[22:25]
	v_mfma_f32_16x16x32_bf16 v[18:21], v[164:167], v[198:201], v[18:21]
	s_setprio 0
	s_barrier
	s_add_u32 s28, s28, 0x80080
	s_addc_u32 s29, s29, 0
	s_add_i32 s30, s30, s35
	v_lshl_add_u64 v[152:153], s[28:29], 0, v[132:133]
	s_mov_b32 m0, s30
	s_nop 0
	global_load_lds_dwordx4 v[152:153], off
	v_lshl_add_u64 v[152:153], s[28:29], 0, v[136:137]
	s_add_i32 m0, s30, 0x2000
	s_nop 0
	global_load_lds_dwordx4 v[152:153], off
	s_waitcnt vmcnt(6)
	s_barrier
	s_setprio 1
	v_mfma_f32_16x16x32_bf16 v[46:49], v[214:217], v[168:171], v[46:49]
	v_mfma_f32_16x16x32_bf16 v[42:45], v[222:225], v[168:171], v[42:45]
	v_mfma_f32_16x16x32_bf16 v[30:33], v[214:217], v[176:179], v[30:33]
	v_mfma_f32_16x16x32_bf16 v[26:29], v[222:225], v[176:179], v[26:29]
	v_mfma_f32_16x16x32_bf16 v[14:17], v[214:217], v[184:187], v[14:17]
	v_mfma_f32_16x16x32_bf16 v[10:13], v[222:225], v[184:187], v[10:13]
	v_mfma_f32_16x16x32_bf16 v[6:9], v[214:217], v[194:197], v[6:9]
	v_mfma_f32_16x16x32_bf16 v[2:5], v[222:225], v[194:197], v[2:5]
	v_mfma_f32_16x16x32_bf16 v[46:49], v[218:221], v[172:175], v[46:49]
	v_mfma_f32_16x16x32_bf16 v[42:45], v[226:229], v[172:175], v[42:45]
	v_mfma_f32_16x16x32_bf16 v[30:33], v[218:221], v[180:183], v[30:33]
	v_mfma_f32_16x16x32_bf16 v[26:29], v[226:229], v[180:183], v[26:29]
	v_mfma_f32_16x16x32_bf16 v[14:17], v[218:221], v[190:193], v[14:17]
	v_mfma_f32_16x16x32_bf16 v[10:13], v[226:229], v[190:193], v[10:13]
	v_mfma_f32_16x16x32_bf16 v[6:9], v[218:221], v[198:201], v[6:9]
	v_mfma_f32_16x16x32_bf16 v[2:5], v[226:229], v[198:201], v[2:5]
	s_setprio 0
	s_add_i32 s54, s54, 2
	s_add_u32 s26, s26, 0x100
	s_addc_u32 s27, s27, 0
	s_add_u32 s52, s52, 0x100
	s_addc_u32 s53, s53, 0
	s_cmp_gt_u32 s54, 29
	s_barrier
	s_cbranch_scc0 .LBB0_1369
	v_lshl_add_u32 v152, s16, 8, v146
	v_lshl_or_b32 v154, s49, 8, v148
	v_ashrrev_i32_e32 v153, 31, v152
	v_ashrrev_i32_e32 v155, 31, v154
	v_lshlrev_b64 v[156:157], 12, v[152:153]
	v_lshl_add_u64 v[156:157], s[96:97], 0, v[156:157]
	v_lshlrev_b64 v[154:155], 1, v[154:155]
	v_lshl_add_u64 v[156:157], v[156:157], 0, v[154:155]
	v_cvt_pk_bf16_f32 v62, v62, v63
	v_cvt_pk_bf16_f32 v63, v64, v65
	v_cvt_pk_bf16_f32 v64, v58, v59
	v_add_co_u32_e32 v58, vcc, s45, v156
	v_cvt_pk_bf16_f32 v70, v70, v71
	v_cvt_pk_bf16_f32 v71, v72, v73
	v_cvt_pk_bf16_f32 v72, v66, v67
	v_lshl_add_u64 v[66:67], v[156:157], 0, s[6:7]
	v_addc_co_u32_e32 v59, vcc, 0, v157, vcc
	v_cvt_pk_bf16_f32 v46, v46, v47
	v_cvt_pk_bf16_f32 v47, v48, v49
	v_cvt_pk_bf16_f32 v48, v42, v43
	v_cvt_pk_bf16_f32 v49, v44, v45
	v_cvt_pk_bf16_f32 v110, v110, v111
	v_cvt_pk_bf16_f32 v111, v112, v113
	v_cvt_pk_bf16_f32 v112, v106, v107
	v_or_b32_e32 v106, 16, v152
	global_store_dwordx4 v[66:67], v[46:49], off offset:256
	v_ashrrev_i32_e32 v107, 31, v106
	v_cvt_pk_bf16_f32 v94, v94, v95
	v_add_co_u32_e32 v48, vcc, s46, v156
	v_cvt_pk_bf16_f32 v95, v96, v97
	v_cvt_pk_bf16_f32 v96, v90, v91
	v_or_b32_e32 v90, 32, v152
	v_lshl_add_u64 v[46:47], v[156:157], 0, s[10:11]
	v_addc_co_u32_e32 v49, vcc, 0, v157, vcc
	v_cvt_pk_bf16_f32 v30, v30, v31
	v_cvt_pk_bf16_f32 v31, v32, v33
	v_cvt_pk_bf16_f32 v32, v26, v27
	v_cvt_pk_bf16_f32 v33, v28, v29
	v_lshlrev_b64 v[106:107], 12, v[106:107]
	v_ashrrev_i32_e32 v91, 31, v90
	v_cvt_pk_bf16_f32 v78, v78, v79
	v_cvt_pk_bf16_f32 v79, v80, v81
	v_cvt_pk_bf16_f32 v80, v74, v75
	v_or_b32_e32 v74, 48, v152
	global_store_dwordx4 v[46:47], v[30:33], off offset:256
	v_cvt_pk_bf16_f32 v113, v108, v109
	v_lshl_add_u64 v[106:107], s[96:97], 0, v[106:107]
	v_add_co_u32_e32 v32, vcc, s47, v156
	v_lshlrev_b64 v[90:91], 12, v[90:91]
	v_ashrrev_i32_e32 v75, 31, v74
	v_lshl_add_u64 v[30:31], v[156:157], 0, s[12:13]
	v_addc_co_u32_e32 v33, vcc, 0, v157, vcc
	v_cvt_pk_bf16_f32 v14, v14, v15
	v_cvt_pk_bf16_f32 v15, v16, v17
	v_cvt_pk_bf16_f32 v16, v10, v11
	v_cvt_pk_bf16_f32 v17, v12, v13
	global_store_dwordx4 v[156:157], v[110:113], off offset:256
	v_cvt_pk_bf16_f32 v97, v92, v93
	v_lshl_add_u64 v[90:91], s[96:97], 0, v[90:91]
	v_lshl_add_u64 v[110:111], v[106:107], 0, v[154:155]
	v_lshlrev_b64 v[74:75], 12, v[74:75]
	global_store_dwordx4 v[30:31], v[14:17], off offset:256
	global_store_dwordx4 v[110:111], v[94:97], off offset:256
	v_cvt_pk_bf16_f32 v81, v76, v77
	v_add_co_u32_e32 v16, vcc, s48, v156
	v_lshl_add_u64 v[94:95], v[90:91], 0, v[154:155]
	v_lshl_add_u64 v[74:75], s[96:97], 0, v[74:75]
	v_addc_co_u32_e32 v17, vcc, 0, v157, vcc
	v_cvt_pk_bf16_f32 v126, v126, v127
	v_cvt_pk_bf16_f32 v127, v128, v129
	v_cvt_pk_bf16_f32 v128, v122, v123
	v_cvt_pk_bf16_f32 v129, v124, v125
	v_cvt_pk_bf16_f32 v106, v118, v119
	v_cvt_pk_bf16_f32 v107, v120, v121
	v_cvt_pk_bf16_f32 v108, v114, v115
	v_cvt_pk_bf16_f32 v109, v116, v117
	v_cvt_pk_bf16_f32 v90, v102, v103
	v_cvt_pk_bf16_f32 v91, v104, v105
	v_cvt_pk_bf16_f32 v92, v98, v99
	v_cvt_pk_bf16_f32 v93, v100, v101
	global_store_dwordx4 v[94:95], v[78:81], off offset:256
	v_cvt_pk_bf16_f32 v76, v82, v83
	v_cvt_pk_bf16_f32 v77, v84, v85
	v_lshl_add_u64 v[78:79], v[74:75], 0, v[154:155]
	v_cvt_pk_bf16_f32 v74, v86, v87
	v_cvt_pk_bf16_f32 v75, v88, v89
	v_cvt_pk_bf16_f32 v73, v68, v69
	v_cvt_pk_bf16_f32 v65, v60, v61
	v_cvt_pk_bf16_f32 v42, v54, v55
	v_cvt_pk_bf16_f32 v43, v56, v57
	v_cvt_pk_bf16_f32 v44, v50, v51
	v_cvt_pk_bf16_f32 v45, v52, v53
	v_cvt_pk_bf16_f32 v26, v38, v39
	v_cvt_pk_bf16_f32 v27, v40, v41
	v_cvt_pk_bf16_f32 v28, v34, v35
	v_cvt_pk_bf16_f32 v29, v36, v37
	v_lshl_add_u64 v[14:15], v[156:157], 0, s[14:15]
	v_cvt_pk_bf16_f32 v10, v22, v23
	v_cvt_pk_bf16_f32 v11, v24, v25
	v_cvt_pk_bf16_f32 v12, v18, v19
	v_cvt_pk_bf16_f32 v13, v20, v21
	v_cvt_pk_bf16_f32 v6, v6, v7
	v_cvt_pk_bf16_f32 v7, v8, v9
	v_cvt_pk_bf16_f32 v8, v2, v3
	v_cvt_pk_bf16_f32 v9, v4, v5
	s_and_b64 vcc, exec, s[0:1]
	s_mov_b32 s49, s18
	s_mov_b32 s16, s20
	s_mov_b64 s[28:29], s[24:25]
	s_mov_b64 s[26:27], s[22:23]
	global_store_dwordx4 v[156:157], v[126:129], off
	global_store_dwordx4 v[110:111], v[106:109], off
	global_store_dwordx4 v[94:95], v[90:93], off
	global_store_dwordx4 v[78:79], v[74:77], off
	global_store_dwordx4 v[78:79], v[70:73], off offset:256
	global_store_dwordx4 v[58:59], v[62:65], off
	global_store_dwordx4 v[48:49], v[42:45], off
	global_store_dwordx4 v[32:33], v[26:29], off
	global_store_dwordx4 v[16:17], v[10:13], off
	global_store_dwordx4 v[14:15], v[6:9], off offset:256
	s_cbranch_vccz .LBB0_1362
	s_waitcnt vmcnt(0)
	s_cmpk_gt_u32 s2, 0xff
	s_cbranch_scc1 .LBB0_1373
	s_barrier
